# fused LSTM: two independent projection MFMAs (different tiles) per idle window; publish and xin prefetch left in flight across the barrier
# baseline (speedup 1.0000x reference)
_Z12lstm2_kernelPKDF16_PKDv8_DF16_Pf:
	s_load_dwordx4 s[8:11], s[0:1], 0x0
	s_load_dwordx2 s[12:13], s[0:1], 0x10
	s_and_b32 s14, s2, 1
	s_lshr_b32 s15, s2, 1
	v_and_b32_e32 v1, 63, v0
	v_lshrrev_b32_e32 v2, 6, v0
	v_lshrrev_b32_e32 v3, 4, v1
	v_and_b32_e32 v4, 15, v0
	v_lshrrev_b32_e32 v5, 2, v4
	v_and_b32_e32 v6, 3, v0
	v_lshlrev_b32_e32 v7, 4, v1
	v_lshl_add_u32 v8, v2, 13, v7
	v_lshl_add_u32 v9, v2, 14, v7
	s_waitcnt lgkmcnt(0)
	s_lshl_b32 s16, s14, 15
	s_add_u32 s16, s16, 0x64000
	s_add_u32 s16, s10, s16
	s_addc_u32 s17, s11, 0
	s_lshl_b32 s18, s14, 16
	s_add_u32 s18, s18, 0x44000
	s_add_u32 s18, s10, s18
	s_addc_u32 s19, s11, 0
	v_add_u32_e32 v10, 0x1000, v8
	global_load_dwordx4 v[16:19], v8, s[16:17] offset:0
	global_load_dwordx4 v[20:23], v8, s[16:17] offset:1024
	global_load_dwordx4 v[24:27], v8, s[16:17] offset:2048
	global_load_dwordx4 v[28:31], v8, s[16:17] offset:3072
	global_load_dwordx4 v[32:35], v10, s[16:17] offset:0
	global_load_dwordx4 v[36:39], v10, s[16:17] offset:1024
	global_load_dwordx4 v[40:43], v10, s[16:17] offset:2048
	global_load_dwordx4 v[44:47], v10, s[16:17] offset:3072
	v_add_u32_e32 v11, 0x1000, v9
	v_add_u32_e32 v12, 0x2000, v9
	v_add_u32_e32 v13, 0x3000, v9
	global_load_dwordx4 v[48:51], v9, s[18:19] offset:0
	global_load_dwordx4 v[52:55], v9, s[18:19] offset:1024
	global_load_dwordx4 v[56:59], v9, s[18:19] offset:2048
	global_load_dwordx4 v[60:63], v9, s[18:19] offset:3072
	global_load_dwordx4 v[64:67], v11, s[18:19] offset:0
	global_load_dwordx4 v[68:71], v11, s[18:19] offset:1024
	global_load_dwordx4 v[72:75], v11, s[18:19] offset:2048
	global_load_dwordx4 v[76:79], v11, s[18:19] offset:3072
	global_load_dwordx4 v[80:83], v12, s[18:19] offset:0
	global_load_dwordx4 v[84:87], v12, s[18:19] offset:1024
	global_load_dwordx4 v[88:91], v12, s[18:19] offset:2048
	global_load_dwordx4 v[92:95], v12, s[18:19] offset:3072
	global_load_dwordx4 v[96:99], v13, s[18:19] offset:0
	global_load_dwordx4 v[100:103], v13, s[18:19] offset:1024
	global_load_dwordx4 v[104:107], v13, s[18:19] offset:2048
	global_load_dwordx4 v[108:111], v13, s[18:19] offset:3072
	s_lshl_b32 s22, s14, 10
	s_add_u32 s22, s8, s22
	s_addc_u32 s23, s9, 0
	v_lshl_add_u32 v14, v2, 4, v3
	v_lshlrev_b32_e32 v14, 2, v14
	global_load_dword v112, v14, s[22:23] offset:0
	global_load_dword v113, v14, s[22:23] offset:256
	global_load_dword v114, v14, s[22:23] offset:512
	global_load_dword v115, v14, s[22:23] offset:768
	global_load_dword v116, v14, s[22:23] offset:16
	global_load_dword v117, v14, s[22:23] offset:272
	global_load_dword v118, v14, s[22:23] offset:528
	global_load_dword v119, v14, s[22:23] offset:784
	global_load_dword v120, v14, s[22:23] offset:32
	global_load_dword v121, v14, s[22:23] offset:288
	global_load_dword v122, v14, s[22:23] offset:544
	global_load_dword v123, v14, s[22:23] offset:800
	global_load_dword v124, v14, s[22:23] offset:48
	global_load_dword v125, v14, s[22:23] offset:304
	global_load_dword v126, v14, s[22:23] offset:560
	global_load_dword v127, v14, s[22:23] offset:816
	s_add_u32 s24, s8, 0xc808000
	s_addc_u32 s25, s9, 0
	s_lshl_b32 s26, s15, 2
	v_add_u32_e32 v15, s26, v6
	s_cmp_eq_u32 s14, 0
	v_sub_u32_e32 v200, 0x18f, v5
	s_cselect_b64 vcc, -1, 0
	s_nop 1
	v_cndmask_b32_e32 v200, v200, v5, vcc
	v_mov_b32_e32 v201, 0x190
	v_mad_u32_u24 v200, v15, v201, v200
	v_lshlrev_b32_e32 v200, 8, v200
	v_lshl_add_u32 v200, v3, 4, v200
	v_mov_b32_e32 v201, 0
	v_lshl_add_u64 v[228:229], s[24:25], 0, v[200:201]
	s_mov_b32 s28, 0x400
	s_cselect_b32 s20, s28, 0xfffffc00
	s_cselect_b32 s21, 0, -1
	global_load_dwordx4 v[128:131], v[228:229], off offset:0
	global_load_dwordx4 v[132:135], v[228:229], off offset:64
	global_load_dwordx4 v[136:139], v[228:229], off offset:128
	global_load_dwordx4 v[140:143], v[228:229], off offset:192
	v_lshl_add_u64 v[228:229], v[228:229], 0, s[20:21]
	global_load_dwordx4 v[144:147], v[228:229], off offset:0
	global_load_dwordx4 v[148:151], v[228:229], off offset:64
	global_load_dwordx4 v[152:155], v[228:229], off offset:128
	global_load_dwordx4 v[156:159], v[228:229], off offset:192
	v_lshl_add_u64 v[228:229], v[228:229], 0, s[20:21]
	v_mul_u32_u24_e32 v202, 144, v6
	v_lshl_add_u32 v224, v3, 4, v202
	v_lshl_add_u32 v203, v2, 4, v3
	v_lshl_add_u32 v203, v5, 2, v203
	v_lshl_add_u32 v225, v203, 1, v202
	v_mul_u32_u24_e32 v204, 8704, v2
	v_lshlrev_b32_e32 v205, 8, v3
	v_lshl_add_u32 v205, v6, 4, v205
	v_add_u32_e32 v205, 1280, v205
	v_add_u32_e32 v205, v205, v204
	v_lshl_add_u32 v226, v5, 6, v205
	v_mul_u32_u24_e32 v206, 1088, v5
	v_add_u32_e32 v227, v205, v206
	s_lshl_b32 s27, s14, 6
	v_lshl_add_u32 v230, v15, 7, v203
	v_add_u32_e32 v230, s27, v230
	v_lshlrev_b32_e32 v230, 2, v230
	v_mov_b32_e32 v208, 0
	v_lshlrev_b32_e32 v200, 2, v0
	v_lshlrev_b32_e32 v201, 2, v1
	ds_write_b32 v200, v208
	ds_write_b32 v201, v208 offset:1024
	v_mov_b32_e32 v220, 0
	v_mov_b32_e32 v221, 0xff61b1e6
	v_mov_b32_e32 v222, 0x4038aa3b
	v_mov_b32_e32 v215, 0xff61b1e6
	s_waitcnt vmcnt(0)
	v_mfma_f32_16x16x32_f16 v[168:171], v[48:51], v[128:131], v[112:115]
	v_mfma_f32_16x16x32_f16 v[168:171], v[52:55], v[132:135], v[168:171]
	v_mfma_f32_16x16x32_f16 v[168:171], v[56:59], v[136:139], v[168:171]
	v_mfma_f32_16x16x32_f16 v[168:171], v[60:63], v[140:143], v[168:171]
	v_mfma_f32_16x16x32_f16 v[172:175], v[64:67], v[128:131], v[116:119]
	v_mfma_f32_16x16x32_f16 v[172:175], v[68:71], v[132:135], v[172:175]
	v_mfma_f32_16x16x32_f16 v[172:175], v[72:75], v[136:139], v[172:175]
	v_mfma_f32_16x16x32_f16 v[172:175], v[76:79], v[140:143], v[172:175]
	v_mfma_f32_16x16x32_f16 v[176:179], v[80:83], v[128:131], v[120:123]
	v_mfma_f32_16x16x32_f16 v[176:179], v[84:87], v[132:135], v[176:179]
	v_mfma_f32_16x16x32_f16 v[176:179], v[88:91], v[136:139], v[176:179]
	v_mfma_f32_16x16x32_f16 v[176:179], v[92:95], v[140:143], v[176:179]
	v_mfma_f32_16x16x32_f16 v[180:183], v[96:99], v[128:131], v[124:127]
	v_mfma_f32_16x16x32_f16 v[180:183], v[100:103], v[132:135], v[180:183]
	v_mfma_f32_16x16x32_f16 v[180:183], v[104:107], v[136:139], v[180:183]
	v_mfma_f32_16x16x32_f16 v[180:183], v[108:111], v[140:143], v[180:183]
	v_mfma_f32_16x16x32_f16 v[160:163], v[48:51], v[144:147], v[112:115]
	v_mfma_f32_16x16x32_f16 v[164:167], v[64:67], v[144:147], v[116:119]
	v_mfma_f32_16x16x32_f16 v[160:163], v[52:55], v[148:151], v[160:163]
	v_mfma_f32_16x16x32_f16 v[160:163], v[56:59], v[152:155], v[160:163]
	s_nop 7
	ds_write_b128 v227, v[168:171] offset:0
	ds_write_b128 v227, v[172:175] offset:64
	ds_write_b128 v227, v[176:179] offset:128
	ds_write_b128 v227, v[180:183] offset:192
	s_movk_i32 s4, 50
	s_waitcnt lgkmcnt(0)
	s_barrier
	ds_read_b128 v[192:195], v226 offset:0
.Llstm3_loop:
	ds_read_b128 v[184:187], v224 offset:0
	ds_read_b128 v[188:191], v224 offset:64
	v_mfma_f32_16x16x32_f16 v[164:167], v[68:71], v[148:151], v[164:167]
	v_mfma_f32_16x16x32_f16 v[160:163], v[60:63], v[156:159], v[160:163]
	global_load_dwordx4 v[128:131], v[228:229], off offset:0
	global_load_dwordx4 v[132:135], v[228:229], off offset:64
	global_load_dwordx4 v[136:139], v[228:229], off offset:128
	global_load_dwordx4 v[140:143], v[228:229], off offset:192
	v_lshl_add_u64 v[228:229], v[228:229], 0, s[20:21]
	s_waitcnt lgkmcnt(0)
	v_mfma_f32_16x16x32_f16 v[168:171], v[16:19], v[184:187], v[192:195]
	v_mfma_f32_16x16x32_f16 v[172:175], v[24:27], v[184:187], v[192:195]
	v_mfma_f32_16x16x32_f16 v[176:179], v[32:35], v[184:187], v[192:195]
	v_mfma_f32_16x16x32_f16 v[180:183], v[40:43], v[184:187], v[192:195]
	v_mfma_f32_16x16x32_f16 v[168:171], v[20:23], v[188:191], v[168:171]
	v_mfma_f32_16x16x32_f16 v[172:175], v[28:31], v[188:191], v[172:175]
	v_mfma_f32_16x16x32_f16 v[176:179], v[36:39], v[188:191], v[176:179]
	v_max_f32_e32 v221, v221, v215
	s_nop 5
	v_mov_b32_dpp v168, v172 quad_perm:[0,1,2,3] row_mask:0xf bank_mask:0x2
	v_mov_b32_dpp v169, v173 quad_perm:[0,1,2,3] row_mask:0xf bank_mask:0x2
	v_mfma_f32_16x16x32_f16 v[180:183], v[44:47], v[188:191], v[180:183]
	v_mov_b32_dpp v170, v174 quad_perm:[0,1,2,3] row_mask:0xf bank_mask:0x2
	v_mov_b32_dpp v171, v175 quad_perm:[0,1,2,3] row_mask:0xf bank_mask:0x2
	s_nop 5
	v_mov_b32_dpp v176, v180 quad_perm:[0,1,2,3] row_mask:0xf bank_mask:0x8
	v_mov_b32_dpp v177, v181 quad_perm:[0,1,2,3] row_mask:0xf bank_mask:0x8
	v_mov_b32_dpp v178, v182 quad_perm:[0,1,2,3] row_mask:0xf bank_mask:0x8
	v_mov_b32_dpp v168, v176 quad_perm:[0,1,2,3] row_mask:0xf bank_mask:0xc
	v_mov_b32_dpp v169, v177 quad_perm:[0,1,2,3] row_mask:0xf bank_mask:0xc
	v_exp_f32_e32 v200, v168
	v_mov_b32_dpp v170, v178 quad_perm:[0,1,2,3] row_mask:0xf bank_mask:0xc
	v_exp_f32_e32 v201, v169
	v_mov_b32_dpp v179, v183 quad_perm:[0,1,2,3] row_mask:0xf bank_mask:0x8
	v_exp_f32_e32 v202, v170
	v_add_f32_e32 v200, 1.0, v200
	v_add_f32_e32 v201, 1.0, v201
	v_mov_b32_dpp v171, v179 quad_perm:[0,1,2,3] row_mask:0xf bank_mask:0xc
	v_add_f32_e32 v202, 1.0, v202
	v_rcp_f32_e32 v202, v202
	v_exp_f32_e32 v203, v171
	v_rcp_f32_e32 v200, v200
	v_rcp_f32_e32 v201, v201
	v_fmamk_f32 v204, v202, 0xc0b8aa3b, v222
	v_add_f32_e32 v203, 1.0, v203
	v_mul_f32_e32 v205, v200, v204
	v_rcp_f32_e32 v203, v203
	v_fma_f32 v220, v201, v220, v205
	v_exp_f32_e32 v206, v220
	v_mul_f32_e32 v207, -2.0, v203
	v_add_f32_e32 v206, 1.0, v206
	v_rcp_f32_e32 v206, v206
	s_nop 0
	v_fma_mixlo_f16 v208, v206, v207, v203
	ds_write_b16 v225, v208 offset:576
	v_fma_f32 v215, v206, v207, v203
	v_mfma_f32_16x16x32_f16 v[232:235], v[80:83], v[144:147], v[120:123]
	v_mfma_f32_16x16x32_f16 v[164:167], v[72:75], v[152:155], v[164:167]
	ds_write_b128 v227, v[160:163] offset:4352
	ds_read_b128 v[196:199], v226 offset:1088
	s_waitcnt lgkmcnt(2)
	s_barrier
	ds_read_b128 v[184:187], v224 offset:576
	ds_read_b128 v[188:191], v224 offset:640
	v_mfma_f32_16x16x32_f16 v[232:235], v[84:87], v[148:151], v[232:235]
	v_mfma_f32_16x16x32_f16 v[164:167], v[76:79], v[156:159], v[164:167]
	s_waitcnt lgkmcnt(0)
	v_mfma_f32_16x16x32_f16 v[168:171], v[16:19], v[184:187], v[196:199]
	v_mfma_f32_16x16x32_f16 v[172:175], v[24:27], v[184:187], v[196:199]
	v_mfma_f32_16x16x32_f16 v[176:179], v[32:35], v[184:187], v[196:199]
	v_mfma_f32_16x16x32_f16 v[180:183], v[40:43], v[184:187], v[196:199]
	v_mfma_f32_16x16x32_f16 v[168:171], v[20:23], v[188:191], v[168:171]
	v_mfma_f32_16x16x32_f16 v[172:175], v[28:31], v[188:191], v[172:175]
	v_mfma_f32_16x16x32_f16 v[176:179], v[36:39], v[188:191], v[176:179]
	v_max_f32_e32 v221, v221, v215
	s_nop 5
	v_mov_b32_dpp v168, v172 quad_perm:[0,1,2,3] row_mask:0xf bank_mask:0x2
	v_mov_b32_dpp v169, v173 quad_perm:[0,1,2,3] row_mask:0xf bank_mask:0x2
	v_mfma_f32_16x16x32_f16 v[180:183], v[44:47], v[188:191], v[180:183]
	v_mov_b32_dpp v170, v174 quad_perm:[0,1,2,3] row_mask:0xf bank_mask:0x2
	v_mov_b32_dpp v171, v175 quad_perm:[0,1,2,3] row_mask:0xf bank_mask:0x2
	s_nop 5
	v_mov_b32_dpp v176, v180 quad_perm:[0,1,2,3] row_mask:0xf bank_mask:0x8
	v_mov_b32_dpp v177, v181 quad_perm:[0,1,2,3] row_mask:0xf bank_mask:0x8
	v_mov_b32_dpp v178, v182 quad_perm:[0,1,2,3] row_mask:0xf bank_mask:0x8
	v_mov_b32_dpp v168, v176 quad_perm:[0,1,2,3] row_mask:0xf bank_mask:0xc
	v_mov_b32_dpp v169, v177 quad_perm:[0,1,2,3] row_mask:0xf bank_mask:0xc
	v_exp_f32_e32 v200, v168
	v_mov_b32_dpp v170, v178 quad_perm:[0,1,2,3] row_mask:0xf bank_mask:0xc
	v_exp_f32_e32 v201, v169
	v_mov_b32_dpp v179, v183 quad_perm:[0,1,2,3] row_mask:0xf bank_mask:0x8
	v_exp_f32_e32 v202, v170
	v_add_f32_e32 v200, 1.0, v200
	v_add_f32_e32 v201, 1.0, v201
	v_mov_b32_dpp v171, v179 quad_perm:[0,1,2,3] row_mask:0xf bank_mask:0xc
	v_add_f32_e32 v202, 1.0, v202
	v_rcp_f32_e32 v202, v202
	v_exp_f32_e32 v203, v171
	v_rcp_f32_e32 v200, v200
	v_rcp_f32_e32 v201, v201
	v_fmamk_f32 v204, v202, 0xc0b8aa3b, v222
	v_add_f32_e32 v203, 1.0, v203
	v_mul_f32_e32 v205, v200, v204
	v_rcp_f32_e32 v203, v203
	v_fma_f32 v220, v201, v220, v205
	v_exp_f32_e32 v206, v220
	v_mul_f32_e32 v207, -2.0, v203
	v_add_f32_e32 v206, 1.0, v206
	v_rcp_f32_e32 v206, v206
	s_nop 0
	v_fma_mixlo_f16 v208, v206, v207, v203
	ds_write_b16 v225, v208 offset:0
	v_fma_f32 v215, v206, v207, v203
	v_mfma_f32_16x16x32_f16 v[236:239], v[96:99], v[144:147], v[124:127]
	v_mfma_f32_16x16x32_f16 v[232:235], v[88:91], v[152:155], v[232:235]
	ds_write_b128 v227, v[164:167] offset:4416
	ds_read_b128 v[192:195], v226 offset:2176
	s_waitcnt lgkmcnt(2)
	s_barrier
	ds_read_b128 v[184:187], v224 offset:0
	ds_read_b128 v[188:191], v224 offset:64
	v_mfma_f32_16x16x32_f16 v[236:239], v[100:103], v[148:151], v[236:239]
	v_mfma_f32_16x16x32_f16 v[232:235], v[92:95], v[156:159], v[232:235]
	s_waitcnt lgkmcnt(0)
	v_mfma_f32_16x16x32_f16 v[168:171], v[16:19], v[184:187], v[192:195]
	v_mfma_f32_16x16x32_f16 v[172:175], v[24:27], v[184:187], v[192:195]
	v_mfma_f32_16x16x32_f16 v[176:179], v[32:35], v[184:187], v[192:195]
	v_mfma_f32_16x16x32_f16 v[180:183], v[40:43], v[184:187], v[192:195]
	v_mfma_f32_16x16x32_f16 v[168:171], v[20:23], v[188:191], v[168:171]
	v_mfma_f32_16x16x32_f16 v[172:175], v[28:31], v[188:191], v[172:175]
	v_mfma_f32_16x16x32_f16 v[176:179], v[36:39], v[188:191], v[176:179]
	v_max_f32_e32 v221, v221, v215
	s_nop 5
	v_mov_b32_dpp v168, v172 quad_perm:[0,1,2,3] row_mask:0xf bank_mask:0x2
	v_mov_b32_dpp v169, v173 quad_perm:[0,1,2,3] row_mask:0xf bank_mask:0x2
	v_mfma_f32_16x16x32_f16 v[180:183], v[44:47], v[188:191], v[180:183]
	v_mov_b32_dpp v170, v174 quad_perm:[0,1,2,3] row_mask:0xf bank_mask:0x2
	v_mov_b32_dpp v171, v175 quad_perm:[0,1,2,3] row_mask:0xf bank_mask:0x2
	s_nop 5
	v_mov_b32_dpp v176, v180 quad_perm:[0,1,2,3] row_mask:0xf bank_mask:0x8
	v_mov_b32_dpp v177, v181 quad_perm:[0,1,2,3] row_mask:0xf bank_mask:0x8
	v_mov_b32_dpp v178, v182 quad_perm:[0,1,2,3] row_mask:0xf bank_mask:0x8
	v_mov_b32_dpp v168, v176 quad_perm:[0,1,2,3] row_mask:0xf bank_mask:0xc
	v_mov_b32_dpp v169, v177 quad_perm:[0,1,2,3] row_mask:0xf bank_mask:0xc
	v_exp_f32_e32 v200, v168
	v_mov_b32_dpp v170, v178 quad_perm:[0,1,2,3] row_mask:0xf bank_mask:0xc
	v_exp_f32_e32 v201, v169
	v_mov_b32_dpp v179, v183 quad_perm:[0,1,2,3] row_mask:0xf bank_mask:0x8
	v_exp_f32_e32 v202, v170
	v_add_f32_e32 v200, 1.0, v200
	v_add_f32_e32 v201, 1.0, v201
	v_mov_b32_dpp v171, v179 quad_perm:[0,1,2,3] row_mask:0xf bank_mask:0xc
	v_add_f32_e32 v202, 1.0, v202
	v_rcp_f32_e32 v202, v202
	v_exp_f32_e32 v203, v171
	v_rcp_f32_e32 v200, v200
	v_rcp_f32_e32 v201, v201
	v_fmamk_f32 v204, v202, 0xc0b8aa3b, v222
	v_add_f32_e32 v203, 1.0, v203
	v_mul_f32_e32 v205, v200, v204
	v_rcp_f32_e32 v203, v203
	v_fma_f32 v220, v201, v220, v205
	v_exp_f32_e32 v206, v220
	v_mul_f32_e32 v207, -2.0, v203
	v_add_f32_e32 v206, 1.0, v206
	v_rcp_f32_e32 v206, v206
	s_nop 0
	v_fma_mixlo_f16 v208, v206, v207, v203
	ds_write_b16 v225, v208 offset:576
	v_fma_f32 v215, v206, v207, v203
	s_waitcnt vmcnt(0)
	v_mfma_f32_16x16x32_f16 v[160:163], v[48:51], v[128:131], v[112:115]
	v_mfma_f32_16x16x32_f16 v[236:239], v[104:107], v[152:155], v[236:239]
	ds_write_b128 v227, v[232:235] offset:4480
	ds_read_b128 v[196:199], v226 offset:3264
	s_waitcnt lgkmcnt(2)
	s_barrier
	ds_read_b128 v[184:187], v224 offset:576
	ds_read_b128 v[188:191], v224 offset:640
	v_mfma_f32_16x16x32_f16 v[160:163], v[52:55], v[132:135], v[160:163]
	v_mfma_f32_16x16x32_f16 v[236:239], v[108:111], v[156:159], v[236:239]
	s_waitcnt lgkmcnt(0)
	v_mfma_f32_16x16x32_f16 v[168:171], v[16:19], v[184:187], v[196:199]
	v_mfma_f32_16x16x32_f16 v[172:175], v[24:27], v[184:187], v[196:199]
	v_mfma_f32_16x16x32_f16 v[176:179], v[32:35], v[184:187], v[196:199]
	v_mfma_f32_16x16x32_f16 v[180:183], v[40:43], v[184:187], v[196:199]
	v_mfma_f32_16x16x32_f16 v[168:171], v[20:23], v[188:191], v[168:171]
	v_mfma_f32_16x16x32_f16 v[172:175], v[28:31], v[188:191], v[172:175]
	v_mfma_f32_16x16x32_f16 v[176:179], v[36:39], v[188:191], v[176:179]
	v_max_f32_e32 v221, v221, v215
	s_nop 5
	v_mov_b32_dpp v168, v172 quad_perm:[0,1,2,3] row_mask:0xf bank_mask:0x2
	v_mov_b32_dpp v169, v173 quad_perm:[0,1,2,3] row_mask:0xf bank_mask:0x2
	v_mfma_f32_16x16x32_f16 v[180:183], v[44:47], v[188:191], v[180:183]
	v_mov_b32_dpp v170, v174 quad_perm:[0,1,2,3] row_mask:0xf bank_mask:0x2
	v_mov_b32_dpp v171, v175 quad_perm:[0,1,2,3] row_mask:0xf bank_mask:0x2
	s_nop 5
	v_mov_b32_dpp v176, v180 quad_perm:[0,1,2,3] row_mask:0xf bank_mask:0x8
	v_mov_b32_dpp v177, v181 quad_perm:[0,1,2,3] row_mask:0xf bank_mask:0x8
	v_mov_b32_dpp v178, v182 quad_perm:[0,1,2,3] row_mask:0xf bank_mask:0x8
	v_mov_b32_dpp v168, v176 quad_perm:[0,1,2,3] row_mask:0xf bank_mask:0xc
	v_mov_b32_dpp v169, v177 quad_perm:[0,1,2,3] row_mask:0xf bank_mask:0xc
	v_exp_f32_e32 v200, v168
	v_mov_b32_dpp v170, v178 quad_perm:[0,1,2,3] row_mask:0xf bank_mask:0xc
	v_exp_f32_e32 v201, v169
	v_mov_b32_dpp v179, v183 quad_perm:[0,1,2,3] row_mask:0xf bank_mask:0x8
	v_exp_f32_e32 v202, v170
	v_add_f32_e32 v200, 1.0, v200
	v_add_f32_e32 v201, 1.0, v201
	v_mov_b32_dpp v171, v179 quad_perm:[0,1,2,3] row_mask:0xf bank_mask:0xc
	v_add_f32_e32 v202, 1.0, v202
	v_rcp_f32_e32 v202, v202
	v_exp_f32_e32 v203, v171
	v_rcp_f32_e32 v200, v200
	v_rcp_f32_e32 v201, v201
	v_fmamk_f32 v204, v202, 0xc0b8aa3b, v222
	v_add_f32_e32 v203, 1.0, v203
	v_mul_f32_e32 v205, v200, v204
	v_rcp_f32_e32 v203, v203
	v_fma_f32 v220, v201, v220, v205
	v_exp_f32_e32 v206, v220
	v_mul_f32_e32 v207, -2.0, v203
	v_add_f32_e32 v206, 1.0, v206
	v_rcp_f32_e32 v206, v206
	s_nop 0
	v_fma_mixlo_f16 v208, v206, v207, v203
	ds_write_b16 v225, v208 offset:0
	v_fma_f32 v215, v206, v207, v203
	v_mfma_f32_16x16x32_f16 v[164:167], v[64:67], v[128:131], v[116:119]
	v_mfma_f32_16x16x32_f16 v[160:163], v[56:59], v[136:139], v[160:163]
	ds_write_b128 v227, v[236:239] offset:4544
	ds_read_b128 v[192:195], v226 offset:4352
	s_waitcnt lgkmcnt(2)
	s_barrier
	ds_read_b128 v[184:187], v224 offset:0
	ds_read_b128 v[188:191], v224 offset:64
	v_mfma_f32_16x16x32_f16 v[164:167], v[68:71], v[132:135], v[164:167]
	v_mfma_f32_16x16x32_f16 v[160:163], v[60:63], v[140:143], v[160:163]
	global_load_dwordx4 v[144:147], v[228:229], off offset:0
	global_load_dwordx4 v[148:151], v[228:229], off offset:64
	global_load_dwordx4 v[152:155], v[228:229], off offset:128
	global_load_dwordx4 v[156:159], v[228:229], off offset:192
	v_lshl_add_u64 v[228:229], v[228:229], 0, s[20:21]
	s_waitcnt lgkmcnt(0)
	v_mfma_f32_16x16x32_f16 v[168:171], v[16:19], v[184:187], v[192:195]
	v_mfma_f32_16x16x32_f16 v[172:175], v[24:27], v[184:187], v[192:195]
	v_mfma_f32_16x16x32_f16 v[176:179], v[32:35], v[184:187], v[192:195]
	v_mfma_f32_16x16x32_f16 v[180:183], v[40:43], v[184:187], v[192:195]
	v_mfma_f32_16x16x32_f16 v[168:171], v[20:23], v[188:191], v[168:171]
	v_mfma_f32_16x16x32_f16 v[172:175], v[28:31], v[188:191], v[172:175]
	v_mfma_f32_16x16x32_f16 v[176:179], v[36:39], v[188:191], v[176:179]
	v_max_f32_e32 v221, v221, v215
	s_nop 5
	v_mov_b32_dpp v168, v172 quad_perm:[0,1,2,3] row_mask:0xf bank_mask:0x2
	v_mov_b32_dpp v169, v173 quad_perm:[0,1,2,3] row_mask:0xf bank_mask:0x2
	v_mfma_f32_16x16x32_f16 v[180:183], v[44:47], v[188:191], v[180:183]
	v_mov_b32_dpp v170, v174 quad_perm:[0,1,2,3] row_mask:0xf bank_mask:0x2
	v_mov_b32_dpp v171, v175 quad_perm:[0,1,2,3] row_mask:0xf bank_mask:0x2
	s_nop 5
	v_mov_b32_dpp v176, v180 quad_perm:[0,1,2,3] row_mask:0xf bank_mask:0x8
	v_mov_b32_dpp v177, v181 quad_perm:[0,1,2,3] row_mask:0xf bank_mask:0x8
	v_mov_b32_dpp v178, v182 quad_perm:[0,1,2,3] row_mask:0xf bank_mask:0x8
	v_mov_b32_dpp v168, v176 quad_perm:[0,1,2,3] row_mask:0xf bank_mask:0xc
	v_mov_b32_dpp v169, v177 quad_perm:[0,1,2,3] row_mask:0xf bank_mask:0xc
	v_exp_f32_e32 v200, v168
	v_mov_b32_dpp v170, v178 quad_perm:[0,1,2,3] row_mask:0xf bank_mask:0xc
	v_exp_f32_e32 v201, v169
	v_mov_b32_dpp v179, v183 quad_perm:[0,1,2,3] row_mask:0xf bank_mask:0x8
	v_exp_f32_e32 v202, v170
	v_add_f32_e32 v200, 1.0, v200
	v_add_f32_e32 v201, 1.0, v201
	v_mov_b32_dpp v171, v179 quad_perm:[0,1,2,3] row_mask:0xf bank_mask:0xc
	v_add_f32_e32 v202, 1.0, v202
	v_rcp_f32_e32 v202, v202
	v_exp_f32_e32 v203, v171
	v_rcp_f32_e32 v200, v200
	v_rcp_f32_e32 v201, v201
	v_fmamk_f32 v204, v202, 0xc0b8aa3b, v222
	v_add_f32_e32 v203, 1.0, v203
	v_mul_f32_e32 v205, v200, v204
	v_rcp_f32_e32 v203, v203
	v_fma_f32 v220, v201, v220, v205
	v_exp_f32_e32 v206, v220
	v_mul_f32_e32 v207, -2.0, v203
	v_add_f32_e32 v206, 1.0, v206
	v_rcp_f32_e32 v206, v206
	s_nop 0
	v_fma_mixlo_f16 v208, v206, v207, v203
	ds_write_b16 v225, v208 offset:576
	v_fma_f32 v215, v206, v207, v203
	v_mfma_f32_16x16x32_f16 v[232:235], v[80:83], v[128:131], v[120:123]
	v_mfma_f32_16x16x32_f16 v[164:167], v[72:75], v[136:139], v[164:167]
	ds_write_b128 v227, v[160:163] offset:0
	ds_read_b128 v[196:199], v226 offset:5440
	s_waitcnt lgkmcnt(2)
	s_barrier
	ds_read_b128 v[184:187], v224 offset:576
	ds_read_b128 v[188:191], v224 offset:640
	v_mfma_f32_16x16x32_f16 v[232:235], v[84:87], v[132:135], v[232:235]
	v_mfma_f32_16x16x32_f16 v[164:167], v[76:79], v[140:143], v[164:167]
	s_waitcnt lgkmcnt(0)
	v_mfma_f32_16x16x32_f16 v[168:171], v[16:19], v[184:187], v[196:199]
	v_mfma_f32_16x16x32_f16 v[172:175], v[24:27], v[184:187], v[196:199]
	v_mfma_f32_16x16x32_f16 v[176:179], v[32:35], v[184:187], v[196:199]
	v_mfma_f32_16x16x32_f16 v[180:183], v[40:43], v[184:187], v[196:199]
	v_mfma_f32_16x16x32_f16 v[168:171], v[20:23], v[188:191], v[168:171]
	v_mfma_f32_16x16x32_f16 v[172:175], v[28:31], v[188:191], v[172:175]
	v_mfma_f32_16x16x32_f16 v[176:179], v[36:39], v[188:191], v[176:179]
	v_max_f32_e32 v221, v221, v215
	s_nop 5
	v_mov_b32_dpp v168, v172 quad_perm:[0,1,2,3] row_mask:0xf bank_mask:0x2
	v_mov_b32_dpp v169, v173 quad_perm:[0,1,2,3] row_mask:0xf bank_mask:0x2
	v_mfma_f32_16x16x32_f16 v[180:183], v[44:47], v[188:191], v[180:183]
	v_mov_b32_dpp v170, v174 quad_perm:[0,1,2,3] row_mask:0xf bank_mask:0x2
	v_mov_b32_dpp v171, v175 quad_perm:[0,1,2,3] row_mask:0xf bank_mask:0x2
	s_nop 5
	v_mov_b32_dpp v176, v180 quad_perm:[0,1,2,3] row_mask:0xf bank_mask:0x8
	v_mov_b32_dpp v177, v181 quad_perm:[0,1,2,3] row_mask:0xf bank_mask:0x8
	v_mov_b32_dpp v178, v182 quad_perm:[0,1,2,3] row_mask:0xf bank_mask:0x8
	v_mov_b32_dpp v168, v176 quad_perm:[0,1,2,3] row_mask:0xf bank_mask:0xc
	v_mov_b32_dpp v169, v177 quad_perm:[0,1,2,3] row_mask:0xf bank_mask:0xc
	v_exp_f32_e32 v200, v168
	v_mov_b32_dpp v170, v178 quad_perm:[0,1,2,3] row_mask:0xf bank_mask:0xc
	v_exp_f32_e32 v201, v169
	v_mov_b32_dpp v179, v183 quad_perm:[0,1,2,3] row_mask:0xf bank_mask:0x8
	v_exp_f32_e32 v202, v170
	v_add_f32_e32 v200, 1.0, v200
	v_add_f32_e32 v201, 1.0, v201
	v_mov_b32_dpp v171, v179 quad_perm:[0,1,2,3] row_mask:0xf bank_mask:0xc
	v_add_f32_e32 v202, 1.0, v202
	v_rcp_f32_e32 v202, v202
	v_exp_f32_e32 v203, v171
	v_rcp_f32_e32 v200, v200
	v_rcp_f32_e32 v201, v201
	v_fmamk_f32 v204, v202, 0xc0b8aa3b, v222
	v_add_f32_e32 v203, 1.0, v203
	v_mul_f32_e32 v205, v200, v204
	v_rcp_f32_e32 v203, v203
	v_fma_f32 v220, v201, v220, v205
	v_exp_f32_e32 v206, v220
	v_mul_f32_e32 v207, -2.0, v203
	v_add_f32_e32 v206, 1.0, v206
	v_rcp_f32_e32 v206, v206
	s_nop 0
	v_fma_mixlo_f16 v208, v206, v207, v203
	ds_write_b16 v225, v208 offset:0
	v_fma_f32 v215, v206, v207, v203
	v_mfma_f32_16x16x32_f16 v[236:239], v[96:99], v[128:131], v[124:127]
	v_mfma_f32_16x16x32_f16 v[232:235], v[88:91], v[136:139], v[232:235]
	ds_write_b128 v227, v[164:167] offset:64
	ds_read_b128 v[192:195], v226 offset:6528
	s_waitcnt lgkmcnt(2)
	s_barrier
	ds_read_b128 v[184:187], v224 offset:0
	ds_read_b128 v[188:191], v224 offset:64
	v_mfma_f32_16x16x32_f16 v[236:239], v[100:103], v[132:135], v[236:239]
	v_mfma_f32_16x16x32_f16 v[232:235], v[92:95], v[140:143], v[232:235]
	s_waitcnt lgkmcnt(0)
	v_mfma_f32_16x16x32_f16 v[168:171], v[16:19], v[184:187], v[192:195]
	v_mfma_f32_16x16x32_f16 v[172:175], v[24:27], v[184:187], v[192:195]
	v_mfma_f32_16x16x32_f16 v[176:179], v[32:35], v[184:187], v[192:195]
	v_mfma_f32_16x16x32_f16 v[180:183], v[40:43], v[184:187], v[192:195]
	v_mfma_f32_16x16x32_f16 v[168:171], v[20:23], v[188:191], v[168:171]
	v_mfma_f32_16x16x32_f16 v[172:175], v[28:31], v[188:191], v[172:175]
	v_mfma_f32_16x16x32_f16 v[176:179], v[36:39], v[188:191], v[176:179]
	v_max_f32_e32 v221, v221, v215
	s_nop 5
	v_mov_b32_dpp v168, v172 quad_perm:[0,1,2,3] row_mask:0xf bank_mask:0x2
	v_mov_b32_dpp v169, v173 quad_perm:[0,1,2,3] row_mask:0xf bank_mask:0x2
	v_mfma_f32_16x16x32_f16 v[180:183], v[44:47], v[188:191], v[180:183]
	v_mov_b32_dpp v170, v174 quad_perm:[0,1,2,3] row_mask:0xf bank_mask:0x2
	v_mov_b32_dpp v171, v175 quad_perm:[0,1,2,3] row_mask:0xf bank_mask:0x2
	s_nop 5
	v_mov_b32_dpp v176, v180 quad_perm:[0,1,2,3] row_mask:0xf bank_mask:0x8
	v_mov_b32_dpp v177, v181 quad_perm:[0,1,2,3] row_mask:0xf bank_mask:0x8
	v_mov_b32_dpp v178, v182 quad_perm:[0,1,2,3] row_mask:0xf bank_mask:0x8
	v_mov_b32_dpp v168, v176 quad_perm:[0,1,2,3] row_mask:0xf bank_mask:0xc
	v_mov_b32_dpp v169, v177 quad_perm:[0,1,2,3] row_mask:0xf bank_mask:0xc
	v_exp_f32_e32 v200, v168
	v_mov_b32_dpp v170, v178 quad_perm:[0,1,2,3] row_mask:0xf bank_mask:0xc
	v_exp_f32_e32 v201, v169
	v_mov_b32_dpp v179, v183 quad_perm:[0,1,2,3] row_mask:0xf bank_mask:0x8
	v_exp_f32_e32 v202, v170
	v_add_f32_e32 v200, 1.0, v200
	v_add_f32_e32 v201, 1.0, v201
	v_mov_b32_dpp v171, v179 quad_perm:[0,1,2,3] row_mask:0xf bank_mask:0xc
	v_add_f32_e32 v202, 1.0, v202
	v_rcp_f32_e32 v202, v202
	v_exp_f32_e32 v203, v171
	v_rcp_f32_e32 v200, v200
	v_rcp_f32_e32 v201, v201
	v_fmamk_f32 v204, v202, 0xc0b8aa3b, v222
	v_add_f32_e32 v203, 1.0, v203
	v_mul_f32_e32 v205, v200, v204
	v_rcp_f32_e32 v203, v203
	v_fma_f32 v220, v201, v220, v205
	v_exp_f32_e32 v206, v220
	v_mul_f32_e32 v207, -2.0, v203
	v_add_f32_e32 v206, 1.0, v206
	v_rcp_f32_e32 v206, v206
	s_nop 0
	v_fma_mixlo_f16 v208, v206, v207, v203
	ds_write_b16 v225, v208 offset:576
	v_fma_f32 v215, v206, v207, v203
	s_waitcnt vmcnt(0)
	v_mfma_f32_16x16x32_f16 v[160:163], v[48:51], v[144:147], v[112:115]
	v_mfma_f32_16x16x32_f16 v[236:239], v[104:107], v[136:139], v[236:239]
	ds_write_b128 v227, v[232:235] offset:128
	ds_read_b128 v[196:199], v226 offset:7616
	s_waitcnt lgkmcnt(2)
	s_barrier
	ds_read_b128 v[184:187], v224 offset:576
	ds_read_b128 v[188:191], v224 offset:640
	v_mfma_f32_16x16x32_f16 v[160:163], v[52:55], v[148:151], v[160:163]
	v_mfma_f32_16x16x32_f16 v[236:239], v[108:111], v[140:143], v[236:239]
	s_waitcnt lgkmcnt(0)
	v_mfma_f32_16x16x32_f16 v[168:171], v[16:19], v[184:187], v[196:199]
	v_mfma_f32_16x16x32_f16 v[172:175], v[24:27], v[184:187], v[196:199]
	v_mfma_f32_16x16x32_f16 v[176:179], v[32:35], v[184:187], v[196:199]
	v_mfma_f32_16x16x32_f16 v[180:183], v[40:43], v[184:187], v[196:199]
	v_mfma_f32_16x16x32_f16 v[168:171], v[20:23], v[188:191], v[168:171]
	v_mfma_f32_16x16x32_f16 v[172:175], v[28:31], v[188:191], v[172:175]
	v_mfma_f32_16x16x32_f16 v[176:179], v[36:39], v[188:191], v[176:179]
	v_max_f32_e32 v221, v221, v215
	s_nop 5
	v_mov_b32_dpp v168, v172 quad_perm:[0,1,2,3] row_mask:0xf bank_mask:0x2
	v_mov_b32_dpp v169, v173 quad_perm:[0,1,2,3] row_mask:0xf bank_mask:0x2
	v_mfma_f32_16x16x32_f16 v[180:183], v[44:47], v[188:191], v[180:183]
	v_mov_b32_dpp v170, v174 quad_perm:[0,1,2,3] row_mask:0xf bank_mask:0x2
	v_mov_b32_dpp v171, v175 quad_perm:[0,1,2,3] row_mask:0xf bank_mask:0x2
	s_nop 5
	v_mov_b32_dpp v176, v180 quad_perm:[0,1,2,3] row_mask:0xf bank_mask:0x8
	v_mov_b32_dpp v177, v181 quad_perm:[0,1,2,3] row_mask:0xf bank_mask:0x8
	v_mov_b32_dpp v178, v182 quad_perm:[0,1,2,3] row_mask:0xf bank_mask:0x8
	v_mov_b32_dpp v168, v176 quad_perm:[0,1,2,3] row_mask:0xf bank_mask:0xc
	v_mov_b32_dpp v169, v177 quad_perm:[0,1,2,3] row_mask:0xf bank_mask:0xc
	v_exp_f32_e32 v200, v168
	v_mov_b32_dpp v170, v178 quad_perm:[0,1,2,3] row_mask:0xf bank_mask:0xc
	v_exp_f32_e32 v201, v169
	v_mov_b32_dpp v179, v183 quad_perm:[0,1,2,3] row_mask:0xf bank_mask:0x8
	v_exp_f32_e32 v202, v170
	v_add_f32_e32 v200, 1.0, v200
	v_add_f32_e32 v201, 1.0, v201
	v_mov_b32_dpp v171, v179 quad_perm:[0,1,2,3] row_mask:0xf bank_mask:0xc
	v_add_f32_e32 v202, 1.0, v202
	v_rcp_f32_e32 v202, v202
	v_exp_f32_e32 v203, v171
	v_rcp_f32_e32 v200, v200
	v_rcp_f32_e32 v201, v201
	v_fmamk_f32 v204, v202, 0xc0b8aa3b, v222
	v_add_f32_e32 v203, 1.0, v203
	v_mul_f32_e32 v205, v200, v204
	v_rcp_f32_e32 v203, v203
	v_fma_f32 v220, v201, v220, v205
	v_exp_f32_e32 v206, v220
	v_mul_f32_e32 v207, -2.0, v203
	v_add_f32_e32 v206, 1.0, v206
	v_rcp_f32_e32 v206, v206
	s_nop 0
	v_fma_mixlo_f16 v208, v206, v207, v203
	ds_write_b16 v225, v208 offset:0
	v_fma_f32 v215, v206, v207, v203
	v_mfma_f32_16x16x32_f16 v[164:167], v[64:67], v[144:147], v[116:119]
	v_mfma_f32_16x16x32_f16 v[160:163], v[56:59], v[152:155], v[160:163]
	ds_write_b128 v227, v[236:239] offset:192
	ds_read_b128 v[192:195], v226 offset:0
	s_waitcnt lgkmcnt(2)
	s_barrier
	s_sub_u32 s4, s4, 1
	s_cmp_lg_u32 s4, 0
	s_cbranch_scc1 .Llstm3_loop
	v_max_f32_e32 v221, v221, v215
	global_store_dword v230, v221, s[12:13]
	s_endpgm

	.amdhsa_kernel _Z12lstm2_kernelPKDF16_PKDv8_DF16_Pf
		.amdhsa_group_segment_fixed_size 36096
		.amdhsa_private_segment_fixed_size 0
		.amdhsa_kernarg_size 24
		.amdhsa_user_sgpr_count 2
		.amdhsa_user_sgpr_dispatch_ptr 0
		.amdhsa_user_sgpr_queue_ptr 0
		.amdhsa_user_sgpr_kernarg_segment_ptr 1
		.amdhsa_user_sgpr_dispatch_id 0
		.amdhsa_user_sgpr_kernarg_preload_length 0
		.amdhsa_user_sgpr_kernarg_preload_offset 0
		.amdhsa_user_sgpr_private_segment_size 0
		.amdhsa_uses_dynamic_stack 0
		.amdhsa_enable_private_segment 0
		.amdhsa_system_sgpr_workgroup_id_x 1
		.amdhsa_system_sgpr_workgroup_id_y 0
		.amdhsa_system_sgpr_workgroup_id_z 0
		.amdhsa_system_sgpr_workgroup_info 0
		.amdhsa_system_vgpr_workitem_id 0
		.amdhsa_next_free_vgpr 252
		.amdhsa_next_free_sgpr 32
		.amdhsa_accum_offset 252
		.amdhsa_reserve_vcc 1
		.amdhsa_float_round_mode_32 0
		.amdhsa_float_round_mode_16_64 0
		.amdhsa_float_denorm_mode_32 3
		.amdhsa_float_denorm_mode_16_64 3
		.amdhsa_dx10_clamp 1
		.amdhsa_ieee_mode 1
		.amdhsa_fp16_overflow 0
		.amdhsa_tg_split 0
		.amdhsa_exception_fp_ieee_invalid_op 0
		.amdhsa_exception_fp_denorm_src 0
		.amdhsa_exception_fp_ieee_div_zero 0
		.amdhsa_exception_fp_ieee_overflow 0
		.amdhsa_exception_fp_ieee_underflow 0
		.amdhsa_exception_fp_ieee_inexact 0
		.amdhsa_exception_int_div_zero 0
	.end_amdhsa_kernel

amdhsa.kernels:
  - .agpr_count:     0
    .args:
      - .actual_access:  write_only
        .address_space:  global
        .offset:         0
        .size:           8
        .value_kind:     global_buffer
      - .actual_access:  read_only
        .address_space:  global
        .offset:         8
        .size:           8
        .value_kind:     global_buffer
      - .actual_access:  read_only
        .address_space:  global
        .offset:         16
        .size:           8
        .value_kind:     global_buffer
      - .actual_access:  read_only
        .address_space:  global
        .offset:         24
        .size:           8
        .value_kind:     global_buffer
      - .actual_access:  read_only
        .address_space:  global
        .offset:         32
        .size:           8
        .value_kind:     global_buffer
      - .actual_access:  read_only
        .address_space:  global
        .offset:         40
        .size:           8
        .value_kind:     global_buffer
      - .actual_access:  read_only
        .address_space:  global
        .offset:         48
        .size:           8
        .value_kind:     global_buffer
      - .actual_access:  read_only
        .address_space:  global
        .offset:         56
        .size:           8
        .value_kind:     global_buffer
      - .actual_access:  read_only
        .address_space:  global
        .offset:         64
        .size:           8
        .value_kind:     global_buffer
      - .actual_access:  read_only
        .address_space:  global
        .offset:         72
        .size:           8
        .value_kind:     global_buffer
    .group_segment_fixed_size: 0
    .kernarg_segment_align: 8
    .kernarg_segment_size: 80
    .language:       OpenCL C
    .language_version:
      - 2
      - 0
    .max_flat_workgroup_size: 64
    .name:           _Z11prep_kernelPDv8_DF16_PKfS2_S2_S2_S2_S2_S2_S2_S2_
    .private_segment_fixed_size: 0
    .sgpr_count:     20
    .sgpr_spill_count: 0
    .symbol:         _Z11prep_kernelPDv8_DF16_PKfS2_S2_S2_S2_S2_S2_S2_S2_.kd
    .uniform_work_group_size: 1
    .uses_dynamic_stack: false
    .vgpr_count:     18
    .vgpr_spill_count: 0
    .wavefront_size: 64
  - .agpr_count:     0
    .args:
      - .actual_access:  read_only
        .address_space:  global
        .offset:         0
        .size:           8
        .value_kind:     global_buffer
      - .actual_access:  read_only
        .address_space:  global
        .offset:         8
        .size:           8
        .value_kind:     global_buffer
      - .actual_access:  write_only
        .address_space:  global
        .offset:         16
        .size:           8
        .value_kind:     global_buffer
    .group_segment_fixed_size: 0
    .kernarg_segment_align: 8
    .kernarg_segment_size: 24
    .language:       OpenCL C
    .language_version:
      - 2
      - 0
    .max_flat_workgroup_size: 256
    .name:           _Z11init_kernelPKfS0_PDF16_
    .private_segment_fixed_size: 0
    .sgpr_count:     16
    .sgpr_spill_count: 0
    .symbol:         _Z11init_kernelPKfS0_PDF16_.kd
    .uniform_work_group_size: 1
    .uses_dynamic_stack: false
    .vgpr_count:     118
    .vgpr_spill_count: 0
    .wavefront_size: 64
  - .agpr_count:     0
    .args:
      - .actual_access:  read_only
        .address_space:  global
        .offset:         0
        .size:           8
        .value_kind:     global_buffer
      - .actual_access:  write_only
        .address_space:  global
        .offset:         8
        .size:           8
        .value_kind:     global_buffer
      - .actual_access:  read_only
        .address_space:  global
        .offset:         16
        .size:           8
        .value_kind:     global_buffer
      - .actual_access:  read_only
        .address_space:  global
        .offset:         24
        .size:           8
        .value_kind:     global_buffer
      - .actual_access:  read_only
        .address_space:  global
        .offset:         32
        .size:           8
        .value_kind:     global_buffer
      - .actual_access:  read_only
        .address_space:  global
        .offset:         40
        .size:           8
        .value_kind:     global_buffer
      - .actual_access:  read_only
        .address_space:  global
        .offset:         48
        .size:           8
        .value_kind:     global_buffer
      - .offset:         56
        .size:           4
        .value_kind:     by_value
      - .offset:         64
        .size:           4
        .value_kind:     hidden_block_count_x
      - .offset:         68
        .size:           4
        .value_kind:     hidden_block_count_y
      - .offset:         72
        .size:           4
        .value_kind:     hidden_block_count_z
      - .offset:         76
        .size:           2
        .value_kind:     hidden_group_size_x
      - .offset:         78
        .size:           2
        .value_kind:     hidden_group_size_y
      - .offset:         80
        .size:           2
        .value_kind:     hidden_group_size_z
      - .offset:         82
        .size:           2
        .value_kind:     hidden_remainder_x
      - .offset:         84
        .size:           2
        .value_kind:     hidden_remainder_y
      - .offset:         86
        .size:           2
        .value_kind:     hidden_remainder_z
      - .offset:         104
        .size:           8
        .value_kind:     hidden_global_offset_x
      - .offset:         112
        .size:           8
        .value_kind:     hidden_global_offset_y
      - .offset:         120
        .size:           8
        .value_kind:     hidden_global_offset_z
      - .offset:         128
        .size:           2
        .value_kind:     hidden_grid_dims
      - .offset:         184
        .size:           4
        .value_kind:     hidden_dynamic_lds_size
    .group_segment_fixed_size: 0
    .kernarg_segment_align: 8
    .kernarg_segment_size: 320
    .language:       OpenCL C
    .language_version:
      - 2
      - 0
    .max_flat_workgroup_size: 512
    .name:           _Z12xproj_kernelPKDF16_PDF16_PKDv8_DF16_PKfS6_S6_S6_i
    .private_segment_fixed_size: 0
    .sgpr_count:     30
    .sgpr_spill_count: 0
    .symbol:         _Z12xproj_kernelPKDF16_PDF16_PKDv8_DF16_PKfS6_S6_S6_i.kd
    .uniform_work_group_size: 1
    .uses_dynamic_stack: false
    .vgpr_count:     16
    .vgpr_spill_count: 0
    .wavefront_size: 64
  - .agpr_count:     0
    .args:
      - .actual_access:  read_only
        .address_space:  global
        .offset:         0
        .size:           8
        .value_kind:     global_buffer
      - .actual_access:  read_only
        .address_space:  global
        .offset:         8
        .size:           8
        .value_kind:     global_buffer
      - .actual_access:  write_only
        .address_space:  global
        .offset:         16
        .size:           8
        .value_kind:     global_buffer
    .group_segment_fixed_size: 5120
    .kernarg_segment_align: 8
    .kernarg_segment_size: 24
    .language:       OpenCL C
    .language_version:
      - 2
      - 0
    .max_flat_workgroup_size: 1024
    .name:           _Z11lstm_kernelPKDF16_PKDv8_DF16_Pf
    .private_segment_fixed_size: 0
    .sgpr_count:     18
    .sgpr_spill_count: 0
    .symbol:         _Z11lstm_kernelPKDF16_PKDv8_DF16_Pf.kd
    .uniform_work_group_size: 1
    .uses_dynamic_stack: false
    .vgpr_count:     52
    .vgpr_spill_count: 0
    .wavefront_size: 64
  - .agpr_count:     0
    .args:
      - .actual_access:  read_only
        .address_space:  global
        .offset:         0
        .size:           8
        .value_kind:     global_buffer
      - .actual_access:  read_only
        .address_space:  global
        .offset:         8
        .size:           8
        .value_kind:     global_buffer
      - .actual_access:  write_only
        .address_space:  global
        .offset:         16
        .size:           8
        .value_kind:     global_buffer
    .group_segment_fixed_size: 36096
    .kernarg_segment_align: 8
    .kernarg_segment_size: 24
    .language:       OpenCL C
    .language_version:
      - 2
      - 0
    .max_flat_workgroup_size: 256
    .name:           _Z12lstm2_kernelPKDF16_PKDv8_DF16_Pf
    .private_segment_fixed_size: 0
    .sgpr_count:     38
    .sgpr_spill_count: 0
    .symbol:         _Z12lstm2_kernelPKDF16_PKDv8_DF16_Pf.kd
    .uniform_work_group_size: 1
    .uses_dynamic_stack: false
    .vgpr_count:     252
    .vgpr_spill_count: 0
    .wavefront_size: 64
  - .agpr_count:     0
    .args:
      - .address_space:  global
        .offset:         0
        .size:           8
        .value_kind:     global_buffer
      - .actual_access:  write_only
        .address_space:  global
        .offset:         8
        .size:           8
        .value_kind:     global_buffer
      - .address_space:  global
        .offset:         16
        .size:           8
        .value_kind:     global_buffer
      - .address_space:  global
        .offset:         24
        .size:           8
        .value_kind:     global_buffer
      - .actual_access:  read_only
        .address_space:  global
        .offset:         32
        .size:           8
        .value_kind:     global_buffer
      - .actual_access:  read_only
        .address_space:  global
        .offset:         40
        .size:           8
        .value_kind:     global_buffer
      - .actual_access:  read_only
        .address_space:  global
        .offset:         48
        .size:           8
        .value_kind:     global_buffer
      - .offset:         56
        .size:           4
        .value_kind:     by_value
      - .offset:         60
        .size:           4
        .value_kind:     by_value
      - .offset:         64
        .size:           4
        .value_kind:     hidden_block_count_x
      - .offset:         68
        .size:           4
        .value_kind:     hidden_block_count_y
      - .offset:         72
        .size:           4
        .value_kind:     hidden_block_count_z
      - .offset:         76
        .size:           2
        .value_kind:     hidden_group_size_x
      - .offset:         78
        .size:           2
        .value_kind:     hidden_group_size_y
      - .offset:         80
        .size:           2
        .value_kind:     hidden_group_size_z
      - .offset:         82
        .size:           2
        .value_kind:     hidden_remainder_x
      - .offset:         84
        .size:           2
        .value_kind:     hidden_remainder_y
      - .offset:         86
        .size:           2
        .value_kind:     hidden_remainder_z
      - .offset:         104
        .size:           8
        .value_kind:     hidden_global_offset_x
      - .offset:         112
        .size:           8
        .value_kind:     hidden_global_offset_y
      - .offset:         120
        .size:           8
        .value_kind:     hidden_global_offset_z
      - .offset:         128
        .size:           2
        .value_kind:     hidden_grid_dims
      - .offset:         184
        .size:           4
        .value_kind:     hidden_dynamic_lds_size
    .group_segment_fixed_size: 0
    .kernarg_segment_align: 8
    .kernarg_segment_size: 320
    .language:       OpenCL C
    .language_version:
      - 2
      - 0
    .max_flat_workgroup_size: 512
    .name:           _Z10mp2_kernelILb0ELi0EEvPKDF16_PDF16_PKiPKfPKDv8_DF16_S6_S6_ii
    .private_segment_fixed_size: 0
    .sgpr_count:     48
    .sgpr_spill_count: 0
    .symbol:         _Z10mp2_kernelILb0ELi0EEvPKDF16_PDF16_PKiPKfPKDv8_DF16_S6_S6_ii.kd
    .uniform_work_group_size: 1
    .uses_dynamic_stack: false
    .vgpr_count:     244
    .vgpr_spill_count: 0
    .wavefront_size: 64
  - .agpr_count:     0
    .args:
      - .actual_access:  read_only
        .address_space:  global
        .offset:         0
        .size:           8
        .value_kind:     global_buffer
      - .actual_access:  write_only
        .address_space:  global
        .offset:         8
        .size:           8
        .value_kind:     global_buffer
      - .address_space:  global
        .offset:         16
        .size:           8
        .value_kind:     global_buffer
      - .address_space:  global
        .offset:         24
        .size:           8
        .value_kind:     global_buffer
      - .actual_access:  read_only
        .address_space:  global
        .offset:         32
        .size:           8
        .value_kind:     global_buffer
      - .actual_access:  read_only
        .address_space:  global
        .offset:         40
        .size:           8
        .value_kind:     global_buffer
      - .actual_access:  read_only
        .address_space:  global
        .offset:         48
        .size:           8
        .value_kind:     global_buffer
      - .offset:         56
        .size:           4
        .value_kind:     by_value
      - .offset:         60
        .size:           4
        .value_kind:     by_value
      - .offset:         64
        .size:           4
        .value_kind:     hidden_block_count_x
      - .offset:         68
        .size:           4
        .value_kind:     hidden_block_count_y
      - .offset:         72
        .size:           4
        .value_kind:     hidden_block_count_z
      - .offset:         76
        .size:           2
        .value_kind:     hidden_group_size_x
      - .offset:         78
        .size:           2
        .value_kind:     hidden_group_size_y
      - .offset:         80
        .size:           2
        .value_kind:     hidden_group_size_z
      - .offset:         82
        .size:           2
        .value_kind:     hidden_remainder_x
      - .offset:         84
        .size:           2
        .value_kind:     hidden_remainder_y
      - .offset:         86
        .size:           2
        .value_kind:     hidden_remainder_z
      - .offset:         104
        .size:           8
        .value_kind:     hidden_global_offset_x
      - .offset:         112
        .size:           8
        .value_kind:     hidden_global_offset_y
      - .offset:         120
        .size:           8
        .value_kind:     hidden_global_offset_z
      - .offset:         128
        .size:           2
        .value_kind:     hidden_grid_dims
      - .offset:         184
        .size:           4
        .value_kind:     hidden_dynamic_lds_size
    .group_segment_fixed_size: 0
    .kernarg_segment_align: 8
    .kernarg_segment_size: 320
    .language:       OpenCL C
    .language_version:
      - 2
      - 0
    .max_flat_workgroup_size: 512
    .name:           _Z10mp2_kernelILb0ELi1EEvPKDF16_PDF16_PKiPKfPKDv8_DF16_S6_S6_ii
    .private_segment_fixed_size: 0
    .sgpr_count:     30
    .sgpr_spill_count: 0
    .symbol:         _Z10mp2_kernelILb0ELi1EEvPKDF16_PDF16_PKiPKfPKDv8_DF16_S6_S6_ii.kd
    .uniform_work_group_size: 1
    .uses_dynamic_stack: false
    .vgpr_count:     234
    .vgpr_spill_count: 0
    .wavefront_size: 64
  - .agpr_count:     0
    .args:
      - .address_space:  global
        .offset:         0
        .size:           8
        .value_kind:     global_buffer
      - .actual_access:  write_only
        .address_space:  global
        .offset:         8
        .size:           8
        .value_kind:     global_buffer
      - .actual_access:  read_only
        .address_space:  global
        .offset:         16
        .size:           8
        .value_kind:     global_buffer
      - .actual_access:  read_only
        .address_space:  global
        .offset:         24
        .size:           8
        .value_kind:     global_buffer
      - .actual_access:  read_only
        .address_space:  global
        .offset:         32
        .size:           8
        .value_kind:     global_buffer
      - .actual_access:  read_only
        .address_space:  global
        .offset:         40
        .size:           8
        .value_kind:     global_buffer
      - .actual_access:  read_only
        .address_space:  global
        .offset:         48
        .size:           8
        .value_kind:     global_buffer
      - .offset:         56
        .size:           4
        .value_kind:     by_value
      - .offset:         60
        .size:           4
        .value_kind:     by_value
      - .offset:         64
        .size:           4
        .value_kind:     hidden_block_count_x
      - .offset:         68
        .size:           4
        .value_kind:     hidden_block_count_y
      - .offset:         72
        .size:           4
        .value_kind:     hidden_block_count_z
      - .offset:         76
        .size:           2
        .value_kind:     hidden_group_size_x
      - .offset:         78
        .size:           2
        .value_kind:     hidden_group_size_y
      - .offset:         80
        .size:           2
        .value_kind:     hidden_group_size_z
      - .offset:         82
        .size:           2
        .value_kind:     hidden_remainder_x
      - .offset:         84
        .size:           2
        .value_kind:     hidden_remainder_y
      - .offset:         86
        .size:           2
        .value_kind:     hidden_remainder_z
      - .offset:         104
        .size:           8
        .value_kind:     hidden_global_offset_x
      - .offset:         112
        .size:           8
        .value_kind:     hidden_global_offset_y
      - .offset:         120
        .size:           8
        .value_kind:     hidden_global_offset_z
      - .offset:         128
        .size:           2
        .value_kind:     hidden_grid_dims
      - .offset:         184
        .size:           4
        .value_kind:     hidden_dynamic_lds_size
    .group_segment_fixed_size: 0
    .kernarg_segment_align: 8
    .kernarg_segment_size: 320
    .language:       OpenCL C
    .language_version:
      - 2
      - 0
    .max_flat_workgroup_size: 512
    .name:           _Z9mp_kernelILi1EEvPKDF16_PDF16_PKiPKfPKDv8_DF16_S6_S6_ii
    .private_segment_fixed_size: 0
    .sgpr_count:     46
    .sgpr_spill_count: 0
    .symbol:         _Z9mp_kernelILi1EEvPKDF16_PDF16_PKiPKfPKDv8_DF16_S6_S6_ii.kd
    .uniform_work_group_size: 1
    .uses_dynamic_stack: false
    .vgpr_count:     70
    .vgpr_spill_count: 0
    .wavefront_size: 64
  - .agpr_count:     0
    .args:
      - .address_space:  global
        .offset:         0
        .size:           8
        .value_kind:     global_buffer
      - .actual_access:  write_only
        .address_space:  global
        .offset:         8
        .size:           8
        .value_kind:     global_buffer
      - .address_space:  global
        .offset:         16
        .size:           8
        .value_kind:     global_buffer
      - .address_space:  global
        .offset:         24
        .size:           8
        .value_kind:     global_buffer
      - .actual_access:  read_only
        .address_space:  global
        .offset:         32
        .size:           8
        .value_kind:     global_buffer
      - .actual_access:  read_only
        .address_space:  global
        .offset:         40
        .size:           8
        .value_kind:     global_buffer
      - .actual_access:  read_only
        .address_space:  global
        .offset:         48
        .size:           8
        .value_kind:     global_buffer
      - .offset:         56
        .size:           4
        .value_kind:     by_value
      - .offset:         60
        .size:           4
        .value_kind:     by_value
      - .offset:         64
        .size:           4
        .value_kind:     hidden_block_count_x
      - .offset:         68
        .size:           4
        .value_kind:     hidden_block_count_y
      - .offset:         72
        .size:           4
        .value_kind:     hidden_block_count_z
      - .offset:         76
        .size:           2
        .value_kind:     hidden_group_size_x
      - .offset:         78
        .size:           2
        .value_kind:     hidden_group_size_y
      - .offset:         80
        .size:           2
        .value_kind:     hidden_group_size_z
      - .offset:         82
        .size:           2
        .value_kind:     hidden_remainder_x
      - .offset:         84
        .size:           2
        .value_kind:     hidden_remainder_y
      - .offset:         86
        .size:           2
        .value_kind:     hidden_remainder_z
      - .offset:         104
        .size:           8
        .value_kind:     hidden_global_offset_x
      - .offset:         112
        .size:           8
        .value_kind:     hidden_global_offset_y
      - .offset:         120
        .size:           8
        .value_kind:     hidden_global_offset_z
      - .offset:         128
        .size:           2
        .value_kind:     hidden_grid_dims
      - .offset:         184
        .size:           4
        .value_kind:     hidden_dynamic_lds_size
    .group_segment_fixed_size: 0
    .kernarg_segment_align: 8
    .kernarg_segment_size: 320
    .language:       OpenCL C
    .language_version:
      - 2
      - 0
    .max_flat_workgroup_size: 512
    .name:           _Z10mp2_kernelILb0ELi2EEvPKDF16_PDF16_PKiPKfPKDv8_DF16_S6_S6_ii
    .private_segment_fixed_size: 0
    .sgpr_count:     32
    .sgpr_spill_count: 0
    .symbol:         _Z10mp2_kernelILb0ELi2EEvPKDF16_PDF16_PKiPKfPKDv8_DF16_S6_S6_ii.kd
    .uniform_work_group_size: 1
    .uses_dynamic_stack: false
    .vgpr_count:     99
    .vgpr_spill_count: 0
    .wavefront_size: 64
